# speedup vs baseline: 1.0046x; 1.0046x over previous
.LBB1_1:
	s_lshl_b32 s6, s36, 14
	s_add_i32 s7, s6, 0
	s_waitcnt vmcnt(0)
	v_add_u32_e32 v112, s7, v175
	s_waitcnt lgkmcnt(0)
	s_barrier
	ds_read_b128 v[64:67], v112
	ds_read_b128 v[68:71], v112 offset:8192
	v_add_u32_e32 v113, s7, v176
	v_exp_f32_e32 v96, v96
	v_exp_f32_e32 v97, v97
	v_exp_f32_e32 v98, v98
	s_waitcnt lgkmcnt(1)
	v_mfma_f32_32x32x16_f16 v[80:95], v[64:67], v[156:159], 0
	ds_read_b128 v[182:185], v113
	ds_read_b128 v[186:189], v113 offset:8192
	v_exp_f32_e32 v99, v99
	v_exp_f32_e32 v181, v102
	v_exp_f32_e32 v218, v103
	v_exp_f32_e32 v219, v104
	v_exp_f32_e32 v220, v105
	s_waitcnt lgkmcnt(2)
	v_mfma_f32_32x32x16_f16 v[64:79], v[68:71], v[156:159], 0
	ds_read_b128 v[190:193], v112 offset:512
	ds_read_b128 v[194:197], v112 offset:8704
	v_exp_f32_e32 v221, v106
	v_exp_f32_e32 v222, v107
	v_exp_f32_e32 v223, v108
	v_exp_f32_e32 v224, v109
	v_exp_f32_e32 v225, v110
	s_waitcnt lgkmcnt(3)
	v_mfma_f32_32x32x16_f16 v[80:95], v[182:185], v[152:155], v[80:95]
	ds_read_b128 v[182:185], v113 offset:512
	ds_read_b128 v[198:201], v113 offset:8704
	v_exp_f32_e32 v226, v111
	v_cvt_pk_f16_f32 v102, v123, v126
	v_cvt_pk_f16_f32 v103, v122, v124
	v_cvt_pk_f16_f32 v104, v119, v121
	v_cvt_pk_f16_f32 v105, v117, v120
	s_waitcnt lgkmcnt(4)
	v_mfma_f32_32x32x16_f16 v[64:79], v[186:189], v[152:155], v[64:79]
	ds_read_b128 v[186:189], v112 offset:1024
	ds_read_b128 v[202:205], v112 offset:9216
	v_cvt_pk_f16_f32 v106, v115, v118
	v_cvt_pk_f16_f32 v107, v114, v116
	v_cvt_pk_f16_f32 v108, v96, v97
	v_cvt_pk_f16_f32 v109, v98, v99
	v_cvt_pk_f16_f32 v111, v181, v218
	s_waitcnt lgkmcnt(5)
	v_mfma_f32_32x32x16_f16 v[80:95], v[190:193], v[148:151], v[80:95]
	ds_read_b128 v[190:193], v113 offset:1024
	ds_read_b128 v[206:209], v113 offset:9216
	s_mov_b32 s4, s36
	v_permlane32_swap_b32_e32 v104, v106
	v_permlane32_swap_b32_e32 v105, v107
	s_waitcnt lgkmcnt(6)
	v_mfma_f32_32x32x16_f16 v[64:79], v[194:197], v[148:151], v[64:79]
	ds_read_b128 v[194:197], v112 offset:1536
	ds_read_b128 v[210:213], v112 offset:9728
	v_exp_f32_e32 v112, v100
	v_add_f32_e32 v100, v180, v127
	v_add_f32_e32 v100, v125, v100
	v_add_f32_e32 v100, v179, v100
	s_waitcnt lgkmcnt(7)
	v_mfma_f32_32x32x16_f16 v[80:95], v[182:185], v[144:147], v[80:95]
	ds_read_b128 v[182:185], v113 offset:1536
	ds_read_b128 v[214:217], v113 offset:9728
	v_add_f32_e32 v100, v123, v100
	v_add_f32_e32 v100, v126, v100
	v_add_f32_e32 v100, v122, v100
	v_add_f32_e32 v100, v124, v100
	v_add_f32_e32 v100, v119, v100
	s_waitcnt lgkmcnt(8)
	v_mfma_f32_32x32x16_f16 v[64:79], v[198:201], v[144:147], v[64:79]
	v_add_f32_e32 v100, v121, v100
	v_add_f32_e32 v100, v117, v100
	v_add_f32_e32 v100, v120, v100
	v_add_f32_e32 v100, v115, v100
	v_add_f32_e32 v100, v118, v100
	v_add_f32_e32 v100, v114, v100
	v_add_f32_e32 v100, v116, v100
	s_waitcnt lgkmcnt(7)
	v_mfma_f32_32x32x16_f16 v[80:95], v[186:189], v[140:143], v[80:95]
	v_add_f32_e32 v100, v96, v100
	v_exp_f32_e32 v113, v101
	v_add_f32_e32 v100, v97, v100
	v_add_f32_e32 v100, v98, v100
	v_add_f32_e32 v100, v99, v100
	v_add_f32_e32 v100, v112, v100
	v_add_f32_e32 v100, v113, v100
	s_waitcnt lgkmcnt(6)
	v_mfma_f32_32x32x16_f16 v[64:79], v[202:205], v[140:143], v[64:79]
	v_add_f32_e32 v100, v181, v100
	v_add_f32_e32 v100, v218, v100
	v_add_f32_e32 v100, v219, v100
	v_add_f32_e32 v100, v220, v100
	v_add_f32_e32 v100, v221, v100
	v_add_f32_e32 v100, v222, v100
	v_add_f32_e32 v100, v223, v100
	s_waitcnt lgkmcnt(5)
	v_mfma_f32_32x32x16_f16 v[80:95], v[190:193], v[136:139], v[80:95]
	v_add_f32_e32 v100, v224, v100
	v_add_f32_e32 v100, v225, v100
	v_add_f32_e32 v177, v226, v100
	v_mov_b32_e32 v178, v177
	v_cvt_pk_f16_f32 v100, v127, v180
	v_cvt_pk_f16_f32 v101, v125, v179
	v_cvt_pk_f16_f32 v110, v112, v113
	s_waitcnt lgkmcnt(4)
	v_mfma_f32_32x32x16_f16 v[64:79], v[206:209], v[136:139], v[64:79]
	v_cvt_pk_f16_f32 v96, v219, v220
	v_cvt_pk_f16_f32 v97, v221, v222
	v_cvt_pk_f16_f32 v98, v223, v224
	v_cvt_pk_f16_f32 v99, v225, v226
	v_permlane32_swap_b32_e32 v177, v178
	v_permlane32_swap_b32_e32 v100, v102
	s_waitcnt lgkmcnt(3)
	v_mfma_f32_32x32x16_f16 v[80:95], v[194:197], v[132:135], v[80:95]
	v_permlane32_swap_b32_e32 v101, v103
	v_permlane32_swap_b32_e32 v108, v110
	v_permlane32_swap_b32_e32 v109, v111
	v_permlane32_swap_b32_e32 v96, v98
	s_waitcnt lgkmcnt(2)
	v_mfma_f32_32x32x16_f16 v[64:79], v[210:213], v[132:135], v[64:79]
	v_permlane32_swap_b32_e32 v97, v99
	v_cmp_gt_f32_e32 vcc, 1.0, v166
	s_waitcnt lgkmcnt(1)
	v_mfma_f32_32x32x16_f16 v[80:95], v[182:185], v[128:131], v[80:95]
	s_waitcnt lgkmcnt(0)
	v_mfma_f32_32x32x16_f16 v[64:79], v[214:217], v[128:131], v[64:79]
	s_cbranch_vccz .LBB1_3
	v_pk_mul_f32 v[62:63], v[166:167], v[62:63] op_sel_hi:[0,1]
	v_pk_mul_f32 v[60:61], v[166:167], v[60:61] op_sel_hi:[0,1]
	v_pk_mul_f32 v[58:59], v[166:167], v[58:59] op_sel_hi:[0,1]
	v_pk_mul_f32 v[56:57], v[166:167], v[56:57] op_sel_hi:[0,1]
	v_pk_mul_f32 v[54:55], v[166:167], v[54:55] op_sel_hi:[0,1]
	v_pk_mul_f32 v[52:53], v[166:167], v[52:53] op_sel_hi:[0,1]
	v_pk_mul_f32 v[50:51], v[166:167], v[50:51] op_sel_hi:[0,1]
	v_pk_mul_f32 v[48:49], v[166:167], v[48:49] op_sel_hi:[0,1]
	v_pk_mul_f32 v[46:47], v[166:167], v[46:47] op_sel_hi:[0,1]
	v_pk_mul_f32 v[44:45], v[166:167], v[44:45] op_sel_hi:[0,1]
	v_pk_mul_f32 v[42:43], v[166:167], v[42:43] op_sel_hi:[0,1]
	v_pk_mul_f32 v[40:41], v[166:167], v[40:41] op_sel_hi:[0,1]
	v_pk_mul_f32 v[38:39], v[166:167], v[38:39] op_sel_hi:[0,1]
	v_pk_mul_f32 v[36:37], v[166:167], v[36:37] op_sel_hi:[0,1]
	v_pk_mul_f32 v[34:35], v[166:167], v[34:35] op_sel_hi:[0,1]
	v_pk_mul_f32 v[32:33], v[166:167], v[32:33] op_sel_hi:[0,1]
	v_pk_mul_f32 v[30:31], v[166:167], v[30:31] op_sel_hi:[0,1]
	v_pk_mul_f32 v[28:29], v[166:167], v[28:29] op_sel_hi:[0,1]
	v_pk_mul_f32 v[26:27], v[166:167], v[26:27] op_sel_hi:[0,1]
	v_pk_mul_f32 v[24:25], v[166:167], v[24:25] op_sel_hi:[0,1]
	v_pk_mul_f32 v[22:23], v[166:167], v[22:23] op_sel_hi:[0,1]
	v_pk_mul_f32 v[20:21], v[166:167], v[20:21] op_sel_hi:[0,1]
	v_pk_mul_f32 v[18:19], v[166:167], v[18:19] op_sel_hi:[0,1]
	v_pk_mul_f32 v[16:17], v[166:167], v[16:17] op_sel_hi:[0,1]
	v_pk_mul_f32 v[14:15], v[166:167], v[14:15] op_sel_hi:[0,1]
	v_pk_mul_f32 v[12:13], v[166:167], v[12:13] op_sel_hi:[0,1]
	v_pk_mul_f32 v[10:11], v[166:167], v[10:11] op_sel_hi:[0,1]
	v_pk_mul_f32 v[8:9], v[166:167], v[8:9] op_sel_hi:[0,1]
	v_pk_mul_f32 v[6:7], v[166:167], v[6:7] op_sel_hi:[0,1]
	v_pk_mul_f32 v[4:5], v[166:167], v[4:5] op_sel_hi:[0,1]
	v_pk_mul_f32 v[2:3], v[166:167], v[2:3] op_sel_hi:[0,1]
	v_pk_mul_f32 v[0:1], v[166:167], v[0:1] op_sel_hi:[0,1]
.LBB1_3:
	s_lshl_b32 s8, s35, 14
	v_add_u32_e32 v114, s8, v173
	v_lshl_add_u64 v[112:113], v[170:171], 0, s[2:3]
	v_readfirstlane_b32 s7, v114
	v_add_u32_e32 v114, 0x400, v114
	s_mov_b32 m0, s7
	v_readfirstlane_b32 s7, v114
	global_load_lds_dwordx4 v[112:113], off
	v_lshl_add_u64 v[112:113], v[170:171], 0, s[20:21]
	s_mov_b32 m0, s7
	s_lshl_b32 s7, s5, 14
	global_load_lds_dwordx4 v[112:113], off
	v_add_u32_e32 v179, s7, v163
	ds_read_b64_tr_b16 v[112:113], v179 offset:0
	v_add_u32_e32 v200, s7, v167
	ds_read_b64_tr_b16 v[114:115], v200 offset:0
	ds_read_b64_tr_b16 v[116:117], v179 offset:0x1000
	ds_read_b64_tr_b16 v[118:119], v200 offset:0x1000
	ds_read_b64_tr_b16 v[120:121], v179 offset:0x2000
	ds_read_b64_tr_b16 v[122:123], v200 offset:0x2000
	ds_read_b64_tr_b16 v[124:125], v179 offset:0x3000
	ds_read_b64_tr_b16 v[126:127], v200 offset:0x3000
	ds_read_b64_tr_b16 v[180:181], v179 offset:0x200
	ds_read_b64_tr_b16 v[182:183], v200 offset:0x200
	ds_read_b64_tr_b16 v[184:185], v179 offset:0x1200
	ds_read_b64_tr_b16 v[186:187], v200 offset:0x1200
	ds_read_b64_tr_b16 v[188:189], v179 offset:0x2200
	ds_read_b64_tr_b16 v[190:191], v200 offset:0x2200
	ds_read_b64_tr_b16 v[192:193], v179 offset:0x3200
	ds_read_b64_tr_b16 v[194:195], v200 offset:0x3200
	s_nop 0
	s_waitcnt lgkmcnt(14)
	v_mfma_f32_32x32x16_f16 v[48:63], v[112:115], v[100:103], v[48:63]
	ds_read_b64_tr_b16 v[112:113], v179 offset:0x400
	ds_read_b64_tr_b16 v[114:115], v200 offset:0x400
	s_waitcnt lgkmcnt(8)
	v_mfma_f32_32x32x16_f16 v[32:47], v[180:183], v[100:103], v[32:47]
	v_mfma_f32_32x32x16_f16 v[48:63], v[116:119], v[104:107], v[48:63]
	ds_read_b64_tr_b16 v[116:117], v179 offset:0x1400
	ds_read_b64_tr_b16 v[118:119], v200 offset:0x1400
	s_waitcnt lgkmcnt(8)
	v_mfma_f32_32x32x16_f16 v[32:47], v[184:187], v[104:107], v[32:47]
	v_mfma_f32_32x32x16_f16 v[48:63], v[120:123], v[108:111], v[48:63]
	ds_read_b64_tr_b16 v[120:121], v179 offset:0x2400
	ds_read_b64_tr_b16 v[122:123], v200 offset:0x2400
	ds_read_b64_tr_b16 v[180:181], v179 offset:0x3400
	ds_read_b64_tr_b16 v[182:183], v200 offset:0x3400
	ds_read_b64_tr_b16 v[184:185], v179 offset:0x600
	ds_read_b64_tr_b16 v[186:187], v200 offset:0x600
	s_waitcnt lgkmcnt(12)
	v_mfma_f32_32x32x16_f16 v[32:47], v[188:191], v[108:111], v[32:47]
	v_mfma_f32_32x32x16_f16 v[48:63], v[124:127], v[96:99], v[48:63]
	ds_read_b64_tr_b16 v[124:125], v179 offset:0x1600
	ds_read_b64_tr_b16 v[126:127], v200 offset:0x1600
	ds_read_b64_tr_b16 v[188:189], v179 offset:0x2600
	ds_read_b64_tr_b16 v[190:191], v200 offset:0x2600
	ds_read_b64_tr_b16 v[196:197], v179 offset:0x3600
	ds_read_b64_tr_b16 v[198:199], v200 offset:0x3600
	s_waitcnt lgkmcnt(15)
	v_mfma_f32_32x32x16_f16 v[32:47], v[192:195], v[96:99], v[32:47]
	v_max_f32_e32 v179, v80, v81
	v_max3_f32 v179, v179, v82, v83
	v_max3_f32 v179, v179, v84, v85
	v_max3_f32 v179, v179, v86, v87
	s_waitcnt lgkmcnt(14)
	v_mfma_f32_32x32x16_f16 v[16:31], v[112:115], v[100:103], v[16:31]
	v_max3_f32 v112, v179, v88, v89
	v_max3_f32 v112, v112, v90, v91
	v_max3_f32 v112, v112, v92, v93
	v_max3_f32 v112, v112, v94, v95
	v_max3_f32 v112, v112, v64, v65
	v_max3_f32 v112, v112, v66, v67
	v_max3_f32 v112, v112, v68, v69
	v_max3_f32 v112, v112, v70, v71
	v_max3_f32 v112, v112, v72, v73
	v_max3_f32 v112, v112, v74, v75
	v_max3_f32 v112, v112, v76, v77
	v_max3_f32 v112, v112, v78, v79
	v_mov_b32_e32 v113, v112
	s_nop 1
	v_permlane32_swap_b32_e32 v112, v113
	v_max_f32_e32 v179, v112, v113
	v_sub_f32_e32 v112, v179, v168
	v_cmp_ge_f32_e32 vcc, s33, v112
	s_cmp_eq_u64 vcc, exec
	s_cselect_b64 vcc, -1, 0
	s_add_i32 s8, s8, 0
	s_waitcnt vmcnt(0)
	v_add_u32_e32 v232, s8, v175
	s_waitcnt lgkmcnt(0)
	s_barrier
	ds_read_b128 v[112:115], v232
	ds_read_b128 v[192:195], v232 offset:8192
	v_mfma_f32_32x32x16_f16 v[0:15], v[184:187], v[100:103], v[0:15]
	v_add_u32_e32 v100, s8, v176
	ds_read_b128 v[184:187], v100
	ds_read_b128 v[200:203], v100 offset:8192
	v_max_f32_e32 v101, v168, v179
	v_sub_f32_e32 v102, v168, v101
	v_exp_f32_e32 v102, v102
	v_mfma_f32_32x32x16_f16 v[16:31], v[116:119], v[104:107], v[16:31]
	ds_read_b128 v[204:207], v232 offset:512
	ds_read_b128 v[208:211], v232 offset:8704
	v_cndmask_b32_e32 v179, v101, v168, vcc
	v_cndmask_b32_e64 v168, v102, 1.0, vcc
	v_sub_f32_e32 v80, v80, v179
	v_sub_f32_e32 v81, v81, v179
	v_sub_f32_e32 v82, v82, v179
	v_mfma_f32_32x32x16_f16 v[0:15], v[124:127], v[104:107], v[0:15]
	ds_read_b128 v[212:215], v100 offset:512
	ds_read_b128 v[216:219], v100 offset:8704
	v_sub_f32_e32 v83, v83, v179
	v_exp_f32_e32 v82, v82
	v_sub_f32_e32 v84, v84, v179
	v_sub_f32_e32 v68, v68, v179
	v_exp_f32_e32 v83, v83
	v_mfma_f32_32x32x16_f16 v[16:31], v[120:123], v[108:111], v[16:31]
	ds_read_b128 v[220:223], v232 offset:1024
	ds_read_b128 v[224:227], v232 offset:9216
	v_sub_f32_e32 v85, v85, v179
	v_exp_f32_e32 v84, v84
	v_sub_f32_e32 v86, v86, v179
	v_exp_f32_e32 v85, v85
	v_sub_f32_e32 v87, v87, v179
	v_mfma_f32_32x32x16_f16 v[0:15], v[188:191], v[108:111], v[0:15]
	ds_read_b128 v[188:191], v100 offset:1024
	ds_read_b128 v[228:231], v100 offset:9216
	v_exp_f32_e32 v86, v86
	v_sub_f32_e32 v88, v88, v179
	v_exp_f32_e32 v87, v87
	v_sub_f32_e32 v89, v89, v179
	v_exp_f32_e32 v88, v88
	v_mfma_f32_32x32x16_f16 v[16:31], v[180:183], v[96:99], v[16:31]
	ds_read_b128 v[180:183], v232 offset:1536
	ds_read_b128 v[232:235], v232 offset:9728
	v_sub_f32_e32 v90, v90, v179
	v_exp_f32_e32 v89, v89
	v_sub_f32_e32 v91, v91, v179
	v_exp_f32_e32 v90, v90
	v_sub_f32_e32 v92, v92, v179
	v_mfma_f32_32x32x16_f16 v[0:15], v[196:199], v[96:99], v[0:15]
	ds_read_b128 v[196:199], v100 offset:1536
	ds_read_b128 v[236:239], v100 offset:9728
	v_exp_f32_e32 v91, v91
	v_sub_f32_e32 v93, v93, v179
	v_exp_f32_e32 v92, v92
	v_sub_f32_e32 v94, v94, v179
	v_exp_f32_e32 v93, v93
	s_waitcnt lgkmcnt(15)
	v_mfma_f32_32x32x16_f16 v[112:127], v[112:115], v[156:159], 0
	v_sub_f32_e32 v95, v95, v179
	v_exp_f32_e32 v94, v94
	v_sub_f32_e32 v64, v64, v179
	v_exp_f32_e32 v95, v95
	v_sub_f32_e32 v65, v65, v179
	v_exp_f32_e32 v64, v64
	v_sub_f32_e32 v66, v66, v179
	s_waitcnt lgkmcnt(14)
	v_mfma_f32_32x32x16_f16 v[96:111], v[192:195], v[156:159], 0
	v_exp_f32_e32 v65, v65
	v_sub_f32_e32 v67, v67, v179
	v_exp_f32_e32 v66, v66
	v_exp_f32_e32 v67, v67
	v_sub_f32_e32 v69, v69, v179
	v_sub_f32_e32 v70, v70, v179
	v_sub_f32_e32 v71, v71, v179
	s_waitcnt lgkmcnt(13)
	v_mfma_f32_32x32x16_f16 v[112:127], v[184:187], v[152:155], v[112:127]
	v_exp_f32_e32 v184, v80
	v_exp_f32_e32 v185, v81
	v_exp_f32_e32 v186, v68
	v_exp_f32_e32 v187, v69
	v_add_f32_e32 v68, v185, v184
	v_add_f32_e32 v68, v82, v68
	s_waitcnt lgkmcnt(12)
	v_mfma_f32_32x32x16_f16 v[96:111], v[200:203], v[152:155], v[96:111]
	v_add_f32_e32 v68, v83, v68
	v_add_f32_e32 v68, v84, v68
	v_add_f32_e32 v68, v85, v68
	v_add_f32_e32 v68, v86, v68
	v_add_f32_e32 v68, v87, v68
	v_add_f32_e32 v68, v88, v68
	v_add_f32_e32 v68, v89, v68
	s_waitcnt lgkmcnt(11)
	v_mfma_f32_32x32x16_f16 v[112:127], v[204:207], v[148:151], v[112:127]
	v_add_f32_e32 v68, v90, v68
	v_add_f32_e32 v68, v91, v68
	v_add_f32_e32 v68, v92, v68
	v_add_f32_e32 v68, v93, v68
	v_add_f32_e32 v68, v94, v68
	v_add_f32_e32 v68, v95, v68
	v_add_f32_e32 v68, v64, v68
	s_waitcnt lgkmcnt(10)
	v_mfma_f32_32x32x16_f16 v[96:111], v[208:211], v[148:151], v[96:111]
	v_add_f32_e32 v68, v65, v68
	v_exp_f32_e32 v192, v70
	v_add_f32_e32 v68, v66, v68
	v_sub_f32_e32 v72, v72, v179
	v_exp_f32_e32 v71, v71
	v_add_f32_e32 v68, v67, v68
	v_sub_f32_e32 v73, v73, v179
	s_waitcnt lgkmcnt(9)
	v_mfma_f32_32x32x16_f16 v[112:127], v[212:215], v[144:147], v[112:127]
	v_exp_f32_e32 v193, v72
	v_add_f32_e32 v68, v186, v68
	v_sub_f32_e32 v74, v74, v179
	v_exp_f32_e32 v194, v73
	v_add_f32_e32 v68, v187, v68
	v_sub_f32_e32 v75, v75, v179
	v_exp_f32_e32 v195, v74
	s_waitcnt lgkmcnt(8)
	v_mfma_f32_32x32x16_f16 v[96:111], v[216:219], v[144:147], v[96:111]
	v_add_f32_e32 v68, v192, v68
	v_sub_f32_e32 v76, v76, v179
	v_exp_f32_e32 v200, v75
	v_add_f32_e32 v68, v71, v68
	v_sub_f32_e32 v77, v77, v179
	v_exp_f32_e32 v201, v76
	v_add_f32_e32 v68, v193, v68
	s_waitcnt lgkmcnt(7)
	v_mfma_f32_32x32x16_f16 v[112:127], v[220:223], v[140:143], v[112:127]
	v_sub_f32_e32 v78, v78, v179
	v_exp_f32_e32 v202, v77
	v_add_f32_e32 v68, v194, v68
	v_sub_f32_e32 v79, v79, v179
	v_exp_f32_e32 v203, v78
	v_add_f32_e32 v68, v195, v68
	v_exp_f32_e32 v204, v79
	s_waitcnt lgkmcnt(6)
	v_mfma_f32_32x32x16_f16 v[96:111], v[224:227], v[140:143], v[96:111]
	v_add_f32_e32 v68, v200, v68
	v_add_f32_e32 v68, v201, v68
	v_add_f32_e32 v68, v202, v68
	v_add_f32_e32 v68, v203, v68
	v_add_f32_e32 v80, v204, v68
	v_mov_b32_e32 v81, v80
	v_cvt_pk_f16_f32 v76, v184, v185
	s_waitcnt lgkmcnt(5)
	v_mfma_f32_32x32x16_f16 v[112:127], v[188:191], v[136:139], v[112:127]
	v_cvt_pk_f16_f32 v77, v82, v83
	v_cvt_pk_f16_f32 v78, v84, v85
	v_cvt_pk_f16_f32 v79, v86, v87
	v_cvt_pk_f16_f32 v72, v88, v89
	v_cvt_pk_f16_f32 v73, v90, v91
	v_cvt_pk_f16_f32 v74, v92, v93
	v_cvt_pk_f16_f32 v75, v94, v95
	s_waitcnt lgkmcnt(4)
	v_mfma_f32_32x32x16_f16 v[96:111], v[228:231], v[136:139], v[96:111]
	v_cvt_pk_f16_f32 v68, v64, v65
	v_cvt_pk_f16_f32 v69, v66, v67
	v_cvt_pk_f16_f32 v70, v186, v187
	v_cvt_pk_f16_f32 v71, v192, v71
	v_cvt_pk_f16_f32 v64, v193, v194
	v_cvt_pk_f16_f32 v65, v195, v200
	v_cvt_pk_f16_f32 v66, v201, v202
	s_waitcnt lgkmcnt(3)
	v_mfma_f32_32x32x16_f16 v[112:127], v[180:183], v[132:135], v[112:127]
	v_cvt_pk_f16_f32 v67, v203, v204
	v_permlane32_swap_b32_e32 v80, v81
	v_permlane32_swap_b32_e32 v76, v78
	v_permlane32_swap_b32_e32 v77, v79
	s_waitcnt lgkmcnt(2)
	v_mfma_f32_32x32x16_f16 v[96:111], v[232:235], v[132:135], v[96:111]
	v_permlane32_swap_b32_e32 v72, v74
	v_permlane32_swap_b32_e32 v73, v75
	v_permlane32_swap_b32_e32 v68, v70
	v_permlane32_swap_b32_e32 v69, v71
	s_waitcnt lgkmcnt(1)
	v_mfma_f32_32x32x16_f16 v[112:127], v[196:199], v[128:131], v[112:127]
	v_permlane32_swap_b32_e32 v64, v66
	v_permlane32_swap_b32_e32 v65, v67
	v_cmp_gt_f32_e32 vcc, 1.0, v168
	s_waitcnt lgkmcnt(0)
	v_mfma_f32_32x32x16_f16 v[96:111], v[236:239], v[128:131], v[96:111]
	s_cbranch_vccz .LBB1_5
	v_pk_mul_f32 v[62:63], v[168:169], v[62:63] op_sel_hi:[0,1]
	v_pk_mul_f32 v[60:61], v[168:169], v[60:61] op_sel_hi:[0,1]
	v_pk_mul_f32 v[58:59], v[168:169], v[58:59] op_sel_hi:[0,1]
	v_pk_mul_f32 v[56:57], v[168:169], v[56:57] op_sel_hi:[0,1]
	v_pk_mul_f32 v[54:55], v[168:169], v[54:55] op_sel_hi:[0,1]
	v_pk_mul_f32 v[52:53], v[168:169], v[52:53] op_sel_hi:[0,1]
	v_pk_mul_f32 v[50:51], v[168:169], v[50:51] op_sel_hi:[0,1]
	v_pk_mul_f32 v[48:49], v[168:169], v[48:49] op_sel_hi:[0,1]
	v_pk_mul_f32 v[46:47], v[168:169], v[46:47] op_sel_hi:[0,1]
	v_pk_mul_f32 v[44:45], v[168:169], v[44:45] op_sel_hi:[0,1]
	v_pk_mul_f32 v[42:43], v[168:169], v[42:43] op_sel_hi:[0,1]
	v_pk_mul_f32 v[40:41], v[168:169], v[40:41] op_sel_hi:[0,1]
	v_pk_mul_f32 v[38:39], v[168:169], v[38:39] op_sel_hi:[0,1]
	v_pk_mul_f32 v[36:37], v[168:169], v[36:37] op_sel_hi:[0,1]
	v_pk_mul_f32 v[34:35], v[168:169], v[34:35] op_sel_hi:[0,1]
	v_pk_mul_f32 v[32:33], v[168:169], v[32:33] op_sel_hi:[0,1]
	v_pk_mul_f32 v[30:31], v[168:169], v[30:31] op_sel_hi:[0,1]
	v_pk_mul_f32 v[28:29], v[168:169], v[28:29] op_sel_hi:[0,1]
	v_pk_mul_f32 v[26:27], v[168:169], v[26:27] op_sel_hi:[0,1]
	v_pk_mul_f32 v[24:25], v[168:169], v[24:25] op_sel_hi:[0,1]
	v_pk_mul_f32 v[22:23], v[168:169], v[22:23] op_sel_hi:[0,1]
	v_pk_mul_f32 v[20:21], v[168:169], v[20:21] op_sel_hi:[0,1]
	v_pk_mul_f32 v[18:19], v[168:169], v[18:19] op_sel_hi:[0,1]
	v_pk_mul_f32 v[16:17], v[168:169], v[16:17] op_sel_hi:[0,1]
	v_pk_mul_f32 v[14:15], v[168:169], v[14:15] op_sel_hi:[0,1]
	v_pk_mul_f32 v[12:13], v[168:169], v[12:13] op_sel_hi:[0,1]
	v_pk_mul_f32 v[10:11], v[168:169], v[10:11] op_sel_hi:[0,1]
	v_pk_mul_f32 v[8:9], v[168:169], v[8:9] op_sel_hi:[0,1]
	v_pk_mul_f32 v[6:7], v[168:169], v[6:7] op_sel_hi:[0,1]
	v_pk_mul_f32 v[4:5], v[168:169], v[4:5] op_sel_hi:[0,1]
	v_pk_mul_f32 v[2:3], v[168:169], v[2:3] op_sel_hi:[0,1]
	v_pk_mul_f32 v[0:1], v[168:169], v[0:1] op_sel_hi:[0,1]
.LBB1_5:
	v_add_f32_e32 v82, v177, v178
	v_fmac_f32_e32 v82, v165, v166
	v_add_f32_e32 v165, v80, v81
	v_fmac_f32_e32 v165, v82, v168
	v_add_u32_e32 v82, s7, v173
	v_add_u32_e32 v83, 0x400, v82
	v_readfirstlane_b32 s7, v82
	v_lshl_add_u64 v[80:81], v[170:171], 0, s[22:23]
	s_mov_b32 m0, s7
	v_readfirstlane_b32 s7, v83
	global_load_lds_dwordx4 v[80:81], off
	s_mov_b32 m0, s7
	v_add_u32_e32 v166, s6, v163
	global_load_lds_dwordx4 v[170:171], off
	ds_read_b64_tr_b16 v[80:81], v166 offset:0
	v_add_u32_e32 v168, s6, v167
	ds_read_b64_tr_b16 v[82:83], v168 offset:0
	ds_read_b64_tr_b16 v[84:85], v166 offset:0x1000
	ds_read_b64_tr_b16 v[86:87], v168 offset:0x1000
	ds_read_b64_tr_b16 v[88:89], v166 offset:0x2000
	ds_read_b64_tr_b16 v[90:91], v168 offset:0x2000
	ds_read_b64_tr_b16 v[92:93], v166 offset:0x3000
	ds_read_b64_tr_b16 v[94:95], v168 offset:0x3000
	ds_read_b64_tr_b16 v[180:181], v166 offset:0x200
	ds_read_b64_tr_b16 v[182:183], v168 offset:0x200
	ds_read_b64_tr_b16 v[184:185], v166 offset:0x1200
	ds_read_b64_tr_b16 v[186:187], v168 offset:0x1200
	ds_read_b64_tr_b16 v[188:189], v166 offset:0x2200
	ds_read_b64_tr_b16 v[190:191], v168 offset:0x2200
	ds_read_b64_tr_b16 v[192:193], v166 offset:0x3200
	ds_read_b64_tr_b16 v[194:195], v168 offset:0x3200
	s_nop 0
	s_waitcnt lgkmcnt(14)
	v_mfma_f32_32x32x16_f16 v[48:63], v[80:83], v[76:79], v[48:63]
	ds_read_b64_tr_b16 v[80:81], v166 offset:0x400
	ds_read_b64_tr_b16 v[82:83], v168 offset:0x400
	s_waitcnt lgkmcnt(8)
	v_mfma_f32_32x32x16_f16 v[32:47], v[180:183], v[76:79], v[32:47]
	v_mfma_f32_32x32x16_f16 v[48:63], v[84:87], v[72:75], v[48:63]
	ds_read_b64_tr_b16 v[84:85], v166 offset:0x1400
	ds_read_b64_tr_b16 v[86:87], v168 offset:0x1400
	s_waitcnt lgkmcnt(8)
	v_mfma_f32_32x32x16_f16 v[32:47], v[184:187], v[72:75], v[32:47]
	v_mfma_f32_32x32x16_f16 v[48:63], v[88:91], v[68:71], v[48:63]
	ds_read_b64_tr_b16 v[88:89], v166 offset:0x2400
	ds_read_b64_tr_b16 v[90:91], v168 offset:0x2400
	ds_read_b64_tr_b16 v[180:181], v166 offset:0x3400
	ds_read_b64_tr_b16 v[182:183], v168 offset:0x3400
	ds_read_b64_tr_b16 v[184:185], v166 offset:0x600
	ds_read_b64_tr_b16 v[186:187], v168 offset:0x600
	s_waitcnt lgkmcnt(12)
	v_mfma_f32_32x32x16_f16 v[32:47], v[188:191], v[68:71], v[32:47]
	v_mfma_f32_32x32x16_f16 v[48:63], v[92:95], v[64:67], v[48:63]
	ds_read_b64_tr_b16 v[92:93], v166 offset:0x1600
	ds_read_b64_tr_b16 v[94:95], v168 offset:0x1600
	ds_read_b64_tr_b16 v[188:189], v166 offset:0x2600
	ds_read_b64_tr_b16 v[190:191], v168 offset:0x2600
	ds_read_b64_tr_b16 v[196:197], v166 offset:0x3600
	ds_read_b64_tr_b16 v[198:199], v168 offset:0x3600
	s_waitcnt lgkmcnt(15)
	v_mfma_f32_32x32x16_f16 v[32:47], v[192:195], v[64:67], v[32:47]
	v_max_f32_e32 v166, v112, v113
	v_max3_f32 v166, v166, v114, v115
	s_waitcnt lgkmcnt(14)
	v_mfma_f32_32x32x16_f16 v[16:31], v[80:83], v[76:79], v[16:31]
	v_max3_f32 v166, v166, v116, v117
	v_max3_f32 v80, v166, v118, v119
	v_max3_f32 v80, v80, v120, v121
	v_max3_f32 v80, v80, v122, v123
	v_max3_f32 v80, v80, v124, v125
	v_max3_f32 v80, v80, v126, v127
	v_max3_f32 v80, v80, v96, v97
	s_waitcnt lgkmcnt(6)
	v_mfma_f32_32x32x16_f16 v[0:15], v[184:187], v[76:79], v[0:15]
	v_max3_f32 v80, v80, v98, v99
	v_max3_f32 v76, v80, v100, v101
	v_max3_f32 v76, v76, v102, v103
	v_max3_f32 v76, v76, v104, v105
	v_max3_f32 v76, v76, v106, v107
	v_max3_f32 v76, v76, v108, v109
	v_max3_f32 v76, v76, v110, v111
	v_mfma_f32_32x32x16_f16 v[16:31], v[84:87], v[72:75], v[16:31]
	v_mov_b32_e32 v77, v76
	s_nop 1
	v_permlane32_swap_b32_e32 v76, v77
	v_max_f32_e32 v76, v76, v77
	v_sub_f32_e32 v77, v76, v179
	s_waitcnt lgkmcnt(4)
	v_mfma_f32_32x32x16_f16 v[0:15], v[92:95], v[72:75], v[0:15]
	v_cmp_ge_f32_e32 vcc, s33, v77
	v_max_f32_e32 v72, v179, v76
	v_sub_f32_e32 v73, v179, v72
	v_exp_f32_e32 v73, v73
	s_cmp_eq_u64 vcc, exec
	s_cselect_b64 vcc, -1, 0
	v_mfma_f32_32x32x16_f16 v[16:31], v[88:91], v[68:71], v[16:31]
	v_cndmask_b32_e32 v168, v72, v179, vcc
	v_cndmask_b32_e64 v166, v73, 1.0, vcc
	v_sub_f32_e32 v72, v112, v168
	v_sub_f32_e32 v73, v113, v168
	v_sub_f32_e32 v74, v114, v168
	v_sub_f32_e32 v75, v115, v168
	v_sub_f32_e32 v76, v116, v168
	s_waitcnt lgkmcnt(2)
	v_mfma_f32_32x32x16_f16 v[0:15], v[188:191], v[68:71], v[0:15]
	v_sub_f32_e32 v77, v117, v168
	v_sub_f32_e32 v78, v118, v168
	v_sub_f32_e32 v68, v119, v168
	v_sub_f32_e32 v69, v120, v168
	v_sub_f32_e32 v70, v121, v168
	v_sub_f32_e32 v71, v122, v168
	v_sub_f32_e32 v79, v123, v168
	v_mfma_f32_32x32x16_f16 v[16:31], v[180:183], v[64:67], v[16:31]
	v_sub_f32_e32 v80, v124, v168
	v_sub_f32_e32 v81, v125, v168
	v_sub_f32_e32 v82, v126, v168
	v_sub_f32_e32 v83, v127, v168
	v_exp_f32_e32 v127, v72
	v_exp_f32_e32 v180, v73
	v_exp_f32_e32 v125, v74
	s_waitcnt lgkmcnt(0)
	v_mfma_f32_32x32x16_f16 v[0:15], v[196:199], v[64:67], v[0:15]
	v_exp_f32_e32 v179, v75
	v_exp_f32_e32 v123, v76
	v_exp_f32_e32 v126, v77
	v_exp_f32_e32 v122, v78
	v_exp_f32_e32 v124, v68
	v_exp_f32_e32 v119, v69
	v_exp_f32_e32 v121, v70
	v_exp_f32_e32 v117, v71
	v_exp_f32_e32 v120, v79
	v_exp_f32_e32 v115, v80
	v_exp_f32_e32 v118, v81
	v_exp_f32_e32 v114, v82
	v_exp_f32_e32 v116, v83
	s_add_i32 s34, s34, 2
	v_sub_f32_e32 v96, v96, v168
	v_sub_f32_e32 v97, v97, v168
	v_sub_f32_e32 v98, v98, v168
	v_sub_f32_e32 v99, v99, v168
	v_sub_f32_e32 v100, v100, v168
	v_sub_f32_e32 v101, v101, v168
	v_sub_f32_e32 v102, v102, v168
	v_sub_f32_e32 v103, v103, v168
	v_sub_f32_e32 v104, v104, v168
	v_sub_f32_e32 v105, v105, v168
	v_sub_f32_e32 v106, v106, v168
	v_sub_f32_e32 v107, v107, v168
	v_sub_f32_e32 v108, v108, v168
	v_sub_f32_e32 v109, v109, v168
	v_sub_f32_e32 v110, v110, v168
	v_sub_f32_e32 v111, v111, v168
	s_cmp_gt_u32 s34, 12
	v_lshl_add_u64 v[170:171], v[170:171], 0, s[30:31]
	s_cbranch_scc1 .LBB1_7
	s_mov_b32 s36, s5
	s_mov_b32 s5, s35
	s_mov_b32 s35, s4
	s_branch .LBB1_1
